# P10: bias vectors loaded before the unit's K loop so the epilogue no longer drains the next unit's prefetch
# baseline (speedup 1.0000x reference)
;     __device__ __forceinline__ void operator()(const f32x4 (&acc)[2][2][4][2], const Unit& u, int wr, int wc, int fr, int fq) const {
;         const int e = u.pn / npn, pnl = u.pn - e * npn; const int tid = threadIdx.x;
;         const int col0 = pnl * BM + wc * 32 + 8 * fq;
;         f32x4 bv[2][2];
; #pragma unroll
;         for (int bj = 0; bj < 2; ++bj)
; #pragma unroll
;             for (int n = 0; n < 2; ++n) bv[bj][n] = *(const f32x4*)(bias + (size_t)e * bias_ld + col0 + bj * HALF + 4 * n);
.LBB0_1146:
	s_ashr_i32 s17, s14, 31
	s_mov_b32 s16, s14
	s_lshl_b64 s[16:17], s[16:17], 19
	s_add_u32 s16, s13, s16
	s_addc_u32 s17, s30, s17
	s_and_b64 s[18:19], s[2:3], exec
	s_cselect_b32 s55, s17, s23
	s_cselect_b32 s56, s16, s22
	s_ashr_i32 s19, s15, 31
	s_mov_b32 s18, s15
	s_lshl_b64 s[18:19], s[18:19], 19
	s_add_u32 s18, s31, s18
	s_addc_u32 s19, s33, s19
	s_and_b64 s[2:3], s[2:3], exec
	s_cselect_b32 s2, s19, s25
	s_cselect_b32 s3, s18, s24
	s_add_u32 s57, s24, 0x100
	v_mov_b32_e32 v34, 0
	v_lshl_add_u64 v[176:177], s[22:23], 0, v[172:173]
	v_lshl_add_u64 v[178:179], s[22:23], 0, v[174:175]
	s_addc_u32 s58, s25, 0
	s_mov_b32 s59, -2
	s_mov_b64 s[24:25], 0
	v_mov_b32_e32 v35, v34
	v_mov_b32_e32 v36, v34
	v_mov_b32_e32 v37, v34
	v_mov_b32_e32 v38, v34
	v_mov_b32_e32 v39, v34
	v_mov_b32_e32 v40, v34
	v_mov_b32_e32 v41, v34
	v_mov_b32_e32 v42, v34
	v_mov_b32_e32 v43, v34
	v_mov_b32_e32 v44, v34
	v_mov_b32_e32 v45, v34
	v_mov_b32_e32 v50, v34
	v_mov_b32_e32 v51, v34
	v_mov_b32_e32 v52, v34
	v_mov_b32_e32 v53, v34
	v_mov_b32_e32 v66, v34
	v_mov_b32_e32 v67, v34
	v_mov_b32_e32 v68, v34
	v_mov_b32_e32 v69, v34
	v_mov_b32_e32 v70, v34
	v_mov_b32_e32 v71, v34
	v_mov_b32_e32 v72, v34
	v_mov_b32_e32 v73, v34
	v_mov_b32_e32 v74, v34
	v_mov_b32_e32 v75, v34
	v_mov_b32_e32 v76, v34
	v_mov_b32_e32 v77, v34
	v_mov_b32_e32 v82, v34
	v_mov_b32_e32 v83, v34
	v_mov_b32_e32 v84, v34
	v_mov_b32_e32 v85, v34
	v_mov_b32_e32 v46, v34
	v_mov_b32_e32 v47, v34
	v_mov_b32_e32 v48, v34
	v_mov_b32_e32 v49, v34
	v_mov_b32_e32 v54, v34
	v_mov_b32_e32 v55, v34
	v_mov_b32_e32 v56, v34
	v_mov_b32_e32 v57, v34
	v_mov_b32_e32 v58, v34
	v_mov_b32_e32 v59, v34
	v_mov_b32_e32 v60, v34
	v_mov_b32_e32 v61, v34
	v_mov_b32_e32 v62, v34
	v_mov_b32_e32 v63, v34
	v_mov_b32_e32 v64, v34
	v_mov_b32_e32 v65, v34
	v_mov_b32_e32 v78, v34
	v_mov_b32_e32 v79, v34
	v_mov_b32_e32 v80, v34
	v_mov_b32_e32 v81, v34
	v_mov_b32_e32 v86, v34
	v_mov_b32_e32 v87, v34
	v_mov_b32_e32 v88, v34
	v_mov_b32_e32 v89, v34
	v_mov_b32_e32 v90, v34
	v_mov_b32_e32 v91, v34
	v_mov_b32_e32 v92, v34
	v_mov_b32_e32 v93, v34
	v_mov_b32_e32 v94, v34
	v_mov_b32_e32 v95, v34
	v_mov_b32_e32 v96, v34
	v_mov_b32_e32 v97, v34
	v_mov_b32_e32 v98, v34
	v_mov_b32_e32 v99, v34
	v_mov_b32_e32 v100, v34
	v_mov_b32_e32 v101, v34
	v_mov_b32_e32 v102, v34
	v_mov_b32_e32 v103, v34
	v_mov_b32_e32 v104, v34
	v_mov_b32_e32 v105, v34
	v_mov_b32_e32 v114, v34
	v_mov_b32_e32 v115, v34
	v_mov_b32_e32 v116, v34
	v_mov_b32_e32 v117, v34
	v_mov_b32_e32 v118, v34
	v_mov_b32_e32 v119, v34
	v_mov_b32_e32 v120, v34
	v_mov_b32_e32 v121, v34
	v_mov_b32_e32 v122, v34
	v_mov_b32_e32 v123, v34
	v_mov_b32_e32 v124, v34
	v_mov_b32_e32 v125, v34
	v_mov_b32_e32 v126, v34
	v_mov_b32_e32 v127, v34
	v_mov_b32_e32 v128, v34
	v_mov_b32_e32 v129, v34
	v_mov_b32_e32 v130, v34
	v_mov_b32_e32 v131, v34
	v_mov_b32_e32 v132, v34
	v_mov_b32_e32 v133, v34
	v_mov_b32_e32 v138, v34
	v_mov_b32_e32 v139, v34
	v_mov_b32_e32 v140, v34
	v_mov_b32_e32 v141, v34
	v_mov_b32_e32 v106, v34
	v_mov_b32_e32 v107, v34
	v_mov_b32_e32 v108, v34
	v_mov_b32_e32 v109, v34
	v_mov_b32_e32 v110, v34
	v_mov_b32_e32 v111, v34
	v_mov_b32_e32 v112, v34
	v_mov_b32_e32 v113, v34
	v_mov_b32_e32 v134, v34
	v_mov_b32_e32 v135, v34
	v_mov_b32_e32 v136, v34
	v_mov_b32_e32 v137, v34
	v_mov_b32_e32 v142, v34
	v_mov_b32_e32 v143, v34
	v_mov_b32_e32 v144, v34
	v_mov_b32_e32 v145, v34
	v_mov_b32_e32 v146, v34
	v_mov_b32_e32 v147, v34
	v_mov_b32_e32 v148, v34
	v_mov_b32_e32 v149, v34
	v_mov_b32_e32 v150, v34
	v_mov_b32_e32 v151, v34
	v_mov_b32_e32 v152, v34
	v_mov_b32_e32 v153, v34
	v_mov_b32_e32 v154, v34
	v_mov_b32_e32 v155, v34
	v_mov_b32_e32 v156, v34
	v_mov_b32_e32 v157, v34
	v_mov_b32_e32 v158, v34
	v_mov_b32_e32 v159, v34
	v_mov_b32_e32 v160, v34
	v_mov_b32_e32 v161, v34
	s_ashr_i32 s98, s21, 31
	s_lshr_b32 s98, s98, 29
	s_add_i32 s98, s21, s98
	s_ashr_i32 s98, s98, 3
	s_lshl_b32 s99, s98, 11
	s_lshl_b32 s100, s21, 8
	s_sub_i32 s100, s100, s99
	s_ashr_i32 s99, s98, 31
	s_lshl_b64 s[98:99], s[98:99], 13
	v_or_b32_e32 v240, s100, v186
	v_readlane_b32 s100, v254, 4
	v_readlane_b32 s101, v254, 5
	v_ashrrev_i32_e32 v241, 31, v240
	s_nop 1
	s_add_u32 s98, s100, s98
	s_addc_u32 s99, s101, s99
	v_lshl_add_u64 v[240:241], v[240:241], 2, s[98:99]
	global_load_dwordx4 v[224:227], v[240:241], off
	global_load_dwordx4 v[228:231], v[240:241], off offset:16
	global_load_dwordx4 v[232:235], v[240:241], off offset:512
	global_load_dwordx4 v[236:239], v[240:241], off offset:528

; #define LAS __attribute__((address_space(3)))
; __device__ __forceinline__ unsigned pk4_fp8(float a, float b, float c, float d) { int w = 0; w = __builtin_amdgcn_cvt_pk_fp8_f32(a, b, w, false); w = __builtin_amdgcn_cvt_pk_fp8_f32(c, d, w, true); return (unsigned)w; }
;     __device__ __forceinline__ void operator()(const f32x4 (&acc)[2][2][4][2], const Unit& u, int wr, int wc, int fr, int fq) const {
;         const int e = u.pn / npn, pnl = u.pn - e * npn; const int tid = threadIdx.x;
;         const int col0 = pnl * BM + wc * 32 + 8 * fq;
;         f32x4 bv[2][2];
; #pragma unroll
;         for (int bj = 0; bj < 2; ++bj)
; #pragma unroll
;             for (int n = 0; n < 2; ++n) bv[bj][n] = *(const f32x4*)(bias + (size_t)e * bias_ld + col0 + bj * HALF + 4 * n);
;         constexpr int PITCH = 272, SLAB = 32 * PITCH;
;         LAS unsigned char* wp = stg + (16 * wr + fr) * PITCH + 32 * wc + 8 * fq;
;         const int rr = tid >> 4, cc = tid & 15; const LAS unsigned char* rp = stg + rr * PITCH + cc * 16;
;         unsigned char* gp = O + (size_t)(u.pm * BM + 64 * (rr >> 4) + (rr & 15)) * ldc + pnl * BM + cc * 16;
; #pragma unroll
;         for (int ai = 0; ai < 2; ++ai)
; #pragma unroll
;             for (int mp = 0; mp < 2; ++mp) {
; #pragma unroll
;                 for (int ms = 0; ms < 2; ++ms)
; #pragma unroll
;                     for (int bj = 0; bj < 2; ++bj) { const int m = 2 * mp + ms; const f32x4 v0 = acc[ai][bj][m][0] * scale + bv[bj][0], v1 = acc[ai][bj][m][1] * scale + bv[bj][1];
;                         u32x2 w; w.x = pk4_fp8(v0[0], v0[1], v0[2], v0[3]); w.y = pk4_fp8(v1[0], v1[1], v1[2], v1[3]);
;                         *(LAS u32x2*)(wp + ms * SLAB + 128 * bj) = w; }
;                 asm volatile("s_waitcnt lgkmcnt(0)" ::: "memory"); __builtin_amdgcn_s_barrier(); asm volatile("" ::: "memory");
; #pragma unroll
;                 for (int ms = 0; ms < 2; ++ms) *(u32x4*)(gp + (size_t)(ai * HALF + (2 * mp + ms) * 16) * ldc) = *(const LAS u32x4*)(rp + ms * SLAB);
;                 asm volatile("s_waitcnt lgkmcnt(0)" ::: "memory"); __builtin_amdgcn_s_barrier(); asm volatile("" ::: "memory");
.LBB0_1150:
	s_ashr_i32 s2, s21, 31
	s_lshr_b32 s2, s2, 29
	s_add_i32 s2, s21, s2
	s_ashr_i32 s2, s2, 3
	s_lshl_b32 s3, s2, 11
	s_lshl_b32 s21, s21, 8
	v_readlane_b32 s56, v254, 0
	s_sub_i32 s22, s21, s3
	s_ashr_i32 s3, s2, 31
	v_readlane_b32 s60, v254, 4
	v_readlane_b32 s61, v254, 5
	s_lshl_b64 s[2:3], s[2:3], 13
	v_readlane_b32 s62, v254, 6
	v_readlane_b32 s63, v254, 7
	s_mov_b64 s[24:25], s[60:61]
	v_or_b32_e32 v2, s22, v186
	s_add_u32 s2, s24, s2
	s_addc_u32 s3, s25, s3
	v_ashrrev_i32_e32 v3, 31, v2
	s_nop 15
	s_nop 15
	v_lshl_add_u64 v[2:3], v[2:3], 2, s[2:3]
	v_pk_mov_b32 v[14:15], v[224:225], v[224:225] op_sel:[0,1]
	v_pk_mov_b32 v[16:17], v[226:227], v[226:227] op_sel:[0,1]
	v_pk_mov_b32 v[10:11], v[228:229], v[228:229] op_sel:[0,1]
	v_pk_mov_b32 v[12:13], v[230:231], v[230:231] op_sel:[0,1]
	v_pk_mov_b32 v[6:7], v[232:233], v[232:233] op_sel:[0,1]
	v_pk_mov_b32 v[8:9], v[234:235], v[234:235] op_sel:[0,1]
	v_pk_mov_b32 v[2:3], v[236:237], v[236:237] op_sel:[0,1]
	v_pk_mov_b32 v[4:5], v[238:239], v[238:239] op_sel:[0,1]
	v_mov_b32_e32 v20, 0
	v_mov_b32_e32 v21, 0
	v_mov_b32_e32 v22, 0
	v_mov_b32_e32 v23, 0
	v_mov_b32_e32 v24, 0
	v_mov_b32_e32 v25, 0
	v_mov_b32_e32 v26, 0
	v_mov_b32_e32 v27, 0
	v_lshl_or_b32 v18, s20, 8, v187
	v_add_u32_e32 v178, 0x2000, v188
	v_ashrrev_i32_e32 v19, 31, v18
	v_lshlrev_b64 v[18:19], 11, v[18:19]
	v_mov_b32_e32 v32, 0
	v_mov_b32_e32 v33, 0
	v_lshl_add_u64 v[18:19], s[4:5], 0, v[18:19]
	s_ashr_i32 s23, s22, 31
	v_lshl_add_u64 v[18:19], v[18:19], 0, s[22:23]
	v_lshl_add_u64 v[18:19], v[18:19], 0, v[170:171]
	v_add_co_u32_e32 v176, vcc, s50, v18
	v_mov_b32_e32 v28, 0
	v_mov_b32_e32 v29, 0
	v_mov_b32_e32 v30, 0
	v_mov_b32_e32 v31, 0
	v_addc_co_u32_e32 v177, vcc, 0, v19, vcc
	s_cmp_eq_u32 s49, s48
	s_mov_b64 s[2:3], -1
	v_readlane_b32 s57, v254, 1
	v_readlane_b32 s58, v254, 2
	v_readlane_b32 s59, v254, 3
	s_mov_b64 s[26:27], s[62:63]
	v_pk_fma_f32 v[158:159], v[158:159], s[12:13], v[14:15] op_sel_hi:[1,0,1]
	v_pk_fma_f32 v[154:155], v[154:155], s[12:13], v[10:11] op_sel_hi:[1,0,1]
	v_pk_fma_f32 v[138:139], v[138:139], s[12:13], v[6:7] op_sel_hi:[1,0,1]
	v_pk_fma_f32 v[130:131], v[130:131], s[12:13], v[2:3] op_sel_hi:[1,0,1]
	v_pk_fma_f32 v[150:151], v[150:151], s[12:13], v[14:15] op_sel_hi:[1,0,1]
	v_pk_fma_f32 v[146:147], v[146:147], s[12:13], v[10:11] op_sel_hi:[1,0,1]
	v_pk_fma_f32 v[126:127], v[126:127], s[12:13], v[6:7] op_sel_hi:[1,0,1]
	v_pk_fma_f32 v[122:123], v[122:123], s[12:13], v[2:3] op_sel_hi:[1,0,1]
	v_cvt_pk_fp8_f32 v20, v158, v159
	v_cvt_pk_fp8_f32 v21, v154, v155
	v_cvt_pk_fp8_f32 v22, v138, v139
	v_cvt_pk_fp8_f32 v23, v130, v131
	v_cvt_pk_fp8_f32 v24, v150, v151
	v_cvt_pk_fp8_f32 v25, v146, v147
	v_cvt_pk_fp8_f32 v26, v126, v127
	v_cvt_pk_fp8_f32 v27, v122, v123
	v_pk_fma_f32 v[160:161], v[160:161], s[12:13], v[16:17] op_sel_hi:[1,0,1]
	v_pk_fma_f32 v[156:157], v[156:157], s[12:13], v[12:13] op_sel_hi:[1,0,1]
	v_pk_fma_f32 v[140:141], v[140:141], s[12:13], v[8:9] op_sel_hi:[1,0,1]
	v_pk_fma_f32 v[132:133], v[132:133], s[12:13], v[4:5] op_sel_hi:[1,0,1]
	v_pk_fma_f32 v[152:153], v[152:153], s[12:13], v[16:17] op_sel_hi:[1,0,1]
	v_pk_fma_f32 v[148:149], v[148:149], s[12:13], v[12:13] op_sel_hi:[1,0,1]
	v_pk_fma_f32 v[128:129], v[128:129], s[12:13], v[8:9] op_sel_hi:[1,0,1]
	v_pk_fma_f32 v[124:125], v[124:125], s[12:13], v[4:5] op_sel_hi:[1,0,1]
	v_cvt_pk_fp8_f32 v20, v160, v161 op_sel:[0,0,1]
	v_cvt_pk_fp8_f32 v21, v156, v157 op_sel:[0,0,1]
	v_cvt_pk_fp8_f32 v22, v140, v141 op_sel:[0,0,1]
	v_cvt_pk_fp8_f32 v23, v132, v133 op_sel:[0,0,1]
	v_cvt_pk_fp8_f32 v24, v152, v153 op_sel:[0,0,1]
	v_cvt_pk_fp8_f32 v25, v148, v149 op_sel:[0,0,1]
	v_cvt_pk_fp8_f32 v26, v128, v129 op_sel:[0,0,1]
	v_cvt_pk_fp8_f32 v27, v124, v125 op_sel:[0,0,1]
	ds_write2_b64 v188, v[20:21], v[22:23] offset1:16
	ds_write2_b64 v178, v[24:25], v[26:27] offset0:64 offset1:80
	s_waitcnt lgkmcnt(0)
	s_barrier
	ds_read_b128 v[20:23], v189
	ds_read_b128 v[24:27], v189 offset:8704
	v_pk_fma_f32 v[110:111], v[110:111], s[12:13], v[14:15] op_sel_hi:[1,0,1]
	v_pk_fma_f32 v[106:107], v[106:107], s[12:13], v[10:11] op_sel_hi:[1,0,1]
	v_cvt_pk_fp8_f32 v32, v110, v111
	v_cvt_pk_fp8_f32 v33, v106, v107
	v_pk_fma_f32 v[142:143], v[142:143], s[12:13], v[14:15] op_sel_hi:[1,0,1]
	v_pk_fma_f32 v[134:135], v[134:135], s[12:13], v[10:11] op_sel_hi:[1,0,1]
	v_pk_fma_f32 v[118:119], v[118:119], s[12:13], v[6:7] op_sel_hi:[1,0,1]
	v_pk_fma_f32 v[114:115], v[114:115], s[12:13], v[2:3] op_sel_hi:[1,0,1]
	s_waitcnt lgkmcnt(1)
	global_store_dwordx4 v[18:19], v[20:23], off
	s_waitcnt lgkmcnt(0)
	global_store_dwordx4 v[176:177], v[24:27], off
	v_cvt_pk_fp8_f32 v28, v142, v143
	v_pk_fma_f32 v[20:21], v[112:113], s[12:13], v[16:17] op_sel_hi:[1,0,1]
	v_pk_fma_f32 v[22:23], v[108:109], s[12:13], v[12:13] op_sel_hi:[1,0,1]
	v_cvt_pk_fp8_f32 v29, v134, v135
	v_cvt_pk_fp8_f32 v30, v118, v119
	v_cvt_pk_fp8_f32 v31, v114, v115
	v_cvt_pk_fp8_f32 v32, v20, v21 op_sel:[0,0,1]
	v_cvt_pk_fp8_f32 v33, v22, v23 op_sel:[0,0,1]
	v_pk_fma_f32 v[20:21], v[102:103], s[12:13], v[6:7] op_sel_hi:[1,0,1]
	v_pk_fma_f32 v[22:23], v[98:99], s[12:13], v[2:3] op_sel_hi:[1,0,1]
	v_mov_b32_e32 v24, 0
	v_mov_b32_e32 v25, 0
	v_cvt_pk_fp8_f32 v24, v20, v21
	v_cvt_pk_fp8_f32 v25, v22, v23
	v_pk_fma_f32 v[144:145], v[144:145], s[12:13], v[16:17] op_sel_hi:[1,0,1]
	v_pk_fma_f32 v[136:137], v[136:137], s[12:13], v[12:13] op_sel_hi:[1,0,1]
	v_pk_fma_f32 v[120:121], v[120:121], s[12:13], v[8:9] op_sel_hi:[1,0,1]
	v_pk_fma_f32 v[116:117], v[116:117], s[12:13], v[4:5] op_sel_hi:[1,0,1]
	v_cvt_pk_fp8_f32 v28, v144, v145 op_sel:[0,0,1]
	v_cvt_pk_fp8_f32 v29, v136, v137 op_sel:[0,0,1]
	v_cvt_pk_fp8_f32 v30, v120, v121 op_sel:[0,0,1]
	v_cvt_pk_fp8_f32 v31, v116, v117 op_sel:[0,0,1]
	v_pk_fma_f32 v[20:21], v[104:105], s[12:13], v[8:9] op_sel_hi:[1,0,1]
	v_pk_fma_f32 v[22:23], v[100:101], s[12:13], v[4:5] op_sel_hi:[1,0,1]
	v_cvt_pk_fp8_f32 v24, v20, v21 op_sel:[0,0,1]
	v_cvt_pk_fp8_f32 v25, v22, v23 op_sel:[0,0,1]
	s_waitcnt lgkmcnt(0)
	s_barrier
; #define LAS __attribute__((address_space(3)))
; __device__ __forceinline__ unsigned pk4_fp8(float a, float b, float c, float d) { int w = 0; w = __builtin_amdgcn_cvt_pk_fp8_f32(a, b, w, false); w = __builtin_amdgcn_cvt_pk_fp8_f32(c, d, w, true); return (unsigned)w; }
;     __device__ __forceinline__ void operator()(const f32x4 (&acc)[2][2][4][2], const Unit& u, int wr, int wc, int fr, int fq) const {
;     ...
;         for (int ai = 0; ai < 2; ++ai)
; #pragma unroll
;             for (int mp = 0; mp < 2; ++mp) {
; #pragma unroll
;                 for (int ms = 0; ms < 2; ++ms)
; #pragma unroll
;                     for (int bj = 0; bj < 2; ++bj) { const int m = 2 * mp + ms; const f32x4 v0 = acc[ai][bj][m][0] * scale + bv[bj][0], v1 = acc[ai][bj][m][1] * scale + bv[bj][1];
;                         u32x2 w; w.x = pk4_fp8(v0[0], v0[1], v0[2], v0[3]); w.y = pk4_fp8(v1[0], v1[1], v1[2], v1[3]);
;                         *(LAS u32x2*)(wp + ms * SLAB + 128 * bj) = w; }
;                 asm volatile("s_waitcnt lgkmcnt(0)" ::: "memory"); __builtin_amdgcn_s_barrier(); asm volatile("" ::: "memory");
; #pragma unroll
;                 for (int ms = 0; ms < 2; ++ms) *(u32x4*)(gp + (size_t)(ai * HALF + (2 * mp + ms) * 16) * ldc) = *(const LAS u32x4*)(rp + ms * SLAB);
;                 asm volatile("s_waitcnt lgkmcnt(0)" ::: "memory"); __builtin_amdgcn_s_barrier(); asm volatile("" ::: "memory");
;             }
	ds_write2_b64 v188, v[28:29], v[30:31] offset1:16
	ds_write2_b64 v178, v[32:33], v[24:25] offset0:64 offset1:80
	s_waitcnt lgkmcnt(0)
	s_barrier
	ds_read_b128 v[20:23], v189
	ds_read_b128 v[24:27], v189 offset:8704
	v_add_co_u32_e32 v28, vcc, s51, v18
	v_mov_b32_e32 v30, 0
	s_nop 0
	v_addc_co_u32_e32 v29, vcc, 0, v19, vcc
	s_waitcnt lgkmcnt(1)
	global_store_dwordx4 v[28:29], v[20:23], off
	v_mov_b32_e32 v28, 0
	v_mov_b32_e32 v29, 0
	v_add_co_u32_e32 v20, vcc, s47, v18
	v_pk_fma_f32 v[22:23], v[90:91], s[12:13], v[10:11] op_sel_hi:[1,0,1]
	s_nop 0
	v_addc_co_u32_e32 v21, vcc, 0, v19, vcc
	s_waitcnt lgkmcnt(0)
	global_store_dwordx4 v[20:21], v[24:27], off
	v_pk_fma_f32 v[20:21], v[94:95], s[12:13], v[14:15] op_sel_hi:[1,0,1]
	v_mov_b32_e32 v31, 0
	v_mov_b32_e32 v24, 0
	v_mov_b32_e32 v25, 0
	v_cvt_pk_fp8_f32 v24, v20, v21
	v_cvt_pk_fp8_f32 v25, v22, v23
	v_pk_fma_f32 v[20:21], v[96:97], s[12:13], v[16:17] op_sel_hi:[1,0,1]
	v_pk_fma_f32 v[22:23], v[92:93], s[12:13], v[12:13] op_sel_hi:[1,0,1]
	v_cvt_pk_fp8_f32 v24, v20, v21 op_sel:[0,0,1]
	v_cvt_pk_fp8_f32 v25, v22, v23 op_sel:[0,0,1]
	v_pk_fma_f32 v[20:21], v[82:83], s[12:13], v[6:7] op_sel_hi:[1,0,1]
	v_pk_fma_f32 v[22:23], v[74:75], s[12:13], v[2:3] op_sel_hi:[1,0,1]
	v_mov_b32_e32 v26, 0
	v_mov_b32_e32 v27, 0
	v_cvt_pk_fp8_f32 v26, v20, v21
	v_cvt_pk_fp8_f32 v27, v22, v23
	v_pk_fma_f32 v[20:21], v[84:85], s[12:13], v[8:9] op_sel_hi:[1,0,1]
	v_pk_fma_f32 v[22:23], v[76:77], s[12:13], v[4:5] op_sel_hi:[1,0,1]
	v_cvt_pk_fp8_f32 v26, v20, v21 op_sel:[0,0,1]
	v_cvt_pk_fp8_f32 v27, v22, v23 op_sel:[0,0,1]
	v_pk_fma_f32 v[20:21], v[86:87], s[12:13], v[14:15] op_sel_hi:[1,0,1]
	v_pk_fma_f32 v[22:23], v[78:79], s[12:13], v[10:11] op_sel_hi:[1,0,1]
	v_cvt_pk_fp8_f32 v28, v20, v21
	v_cvt_pk_fp8_f32 v29, v22, v23
	v_pk_fma_f32 v[20:21], v[88:89], s[12:13], v[16:17] op_sel_hi:[1,0,1]
	v_pk_fma_f32 v[22:23], v[80:81], s[12:13], v[12:13] op_sel_hi:[1,0,1]
	v_cvt_pk_fp8_f32 v28, v20, v21 op_sel:[0,0,1]
	v_cvt_pk_fp8_f32 v29, v22, v23 op_sel:[0,0,1]
	v_pk_fma_f32 v[20:21], v[70:71], s[12:13], v[6:7] op_sel_hi:[1,0,1]
	v_pk_fma_f32 v[22:23], v[66:67], s[12:13], v[2:3] op_sel_hi:[1,0,1]
	v_cvt_pk_fp8_f32 v30, v20, v21
	v_cvt_pk_fp8_f32 v31, v22, v23
	v_pk_fma_f32 v[20:21], v[72:73], s[12:13], v[8:9] op_sel_hi:[1,0,1]
	v_pk_fma_f32 v[22:23], v[68:69], s[12:13], v[4:5] op_sel_hi:[1,0,1]
	v_cvt_pk_fp8_f32 v30, v20, v21 op_sel:[0,0,1]
	v_cvt_pk_fp8_f32 v31, v22, v23 op_sel:[0,0,1]
	s_waitcnt lgkmcnt(0)
	s_barrier
	ds_write2_b64 v188, v[24:25], v[26:27] offset1:16
	ds_write2_b64 v178, v[28:29], v[30:31] offset0:64 offset1:80
	s_waitcnt lgkmcnt(0)
	s_barrier
	ds_read_b128 v[20:23], v189
	ds_read_b128 v[24:27], v189 offset:8704
	v_add_co_u32_e32 v28, vcc, s52, v18
	s_nop 1
	v_addc_co_u32_e32 v29, vcc, 0, v19, vcc
	s_waitcnt lgkmcnt(1)
	global_store_dwordx4 v[28:29], v[20:23], off
	s_nop 1
	v_add_co_u32_e32 v20, vcc, s53, v18
	v_pk_fma_f32 v[22:23], v[58:59], s[12:13], v[10:11] op_sel_hi:[1,0,1]
	s_nop 0
	v_addc_co_u32_e32 v21, vcc, 0, v19, vcc
	s_waitcnt lgkmcnt(0)
	global_store_dwordx4 v[20:21], v[24:27], off
	v_pk_fma_f32 v[20:21], v[62:63], s[12:13], v[14:15] op_sel_hi:[1,0,1]
	v_pk_fma_f32 v[14:15], v[54:55], s[12:13], v[14:15] op_sel_hi:[1,0,1]
	v_mov_b32_e32 v24, 0
	v_cvt_pk_fp8_f32 v24, v20, v21
	v_pk_fma_f32 v[20:21], v[64:65], s[12:13], v[16:17] op_sel_hi:[1,0,1]
	v_mov_b32_e32 v26, 0
	v_mov_b32_e32 v25, 0
	v_cvt_pk_fp8_f32 v24, v20, v21 op_sel:[0,0,1]
	v_pk_fma_f32 v[20:21], v[50:51], s[12:13], v[6:7] op_sel_hi:[1,0,1]
	v_cvt_pk_fp8_f32 v25, v22, v23
	v_cvt_pk_fp8_f32 v26, v20, v21
	v_pk_fma_f32 v[20:21], v[52:53], s[12:13], v[8:9] op_sel_hi:[1,0,1]
	v_pk_fma_f32 v[22:23], v[60:61], s[12:13], v[12:13] op_sel_hi:[1,0,1]
	v_pk_fma_f32 v[10:11], v[46:47], s[12:13], v[10:11] op_sel_hi:[1,0,1]
	v_cvt_pk_fp8_f32 v26, v20, v21 op_sel:[0,0,1]
	v_mov_b32_e32 v20, 0
	v_cvt_pk_fp8_f32 v20, v14, v15
	v_mov_b32_e32 v21, 0
	v_cvt_pk_fp8_f32 v25, v22, v23 op_sel:[0,0,1]
	v_pk_fma_f32 v[22:23], v[42:43], s[12:13], v[2:3] op_sel_hi:[1,0,1]
	v_mov_b32_e32 v27, 0
	v_cvt_pk_fp8_f32 v21, v10, v11
	v_pk_fma_f32 v[10:11], v[56:57], s[12:13], v[16:17] op_sel_hi:[1,0,1]
	v_cvt_pk_fp8_f32 v27, v22, v23
	v_cvt_pk_fp8_f32 v20, v10, v11 op_sel:[0,0,1]
	v_pk_fma_f32 v[6:7], v[38:39], s[12:13], v[6:7] op_sel_hi:[1,0,1]
	v_pk_fma_f32 v[2:3], v[34:35], s[12:13], v[2:3] op_sel_hi:[1,0,1]
	v_mov_b32_e32 v10, 0
	v_mov_b32_e32 v11, 0
	v_cvt_pk_fp8_f32 v10, v6, v7
	v_cvt_pk_fp8_f32 v11, v2, v3
	v_pk_fma_f32 v[22:23], v[44:45], s[12:13], v[4:5] op_sel_hi:[1,0,1]
	v_pk_fma_f32 v[12:13], v[48:49], s[12:13], v[12:13] op_sel_hi:[1,0,1]
	v_cvt_pk_fp8_f32 v27, v22, v23 op_sel:[0,0,1]
	v_pk_fma_f32 v[2:3], v[40:41], s[12:13], v[8:9] op_sel_hi:[1,0,1]
	v_pk_fma_f32 v[4:5], v[36:37], s[12:13], v[4:5] op_sel_hi:[1,0,1]
	v_cvt_pk_fp8_f32 v21, v12, v13 op_sel:[0,0,1]
	v_cvt_pk_fp8_f32 v10, v2, v3 op_sel:[0,0,1]
	v_cvt_pk_fp8_f32 v11, v4, v5 op_sel:[0,0,1]
	s_waitcnt lgkmcnt(0)
	s_barrier
	ds_write2_b64 v188, v[24:25], v[26:27] offset1:16
	ds_write2_b64 v178, v[20:21], v[10:11] offset0:64 offset1:80
	s_waitcnt lgkmcnt(0)
	s_barrier
	ds_read_b128 v[2:5], v189
	ds_read_b128 v[6:9], v189 offset:8704
	v_add_co_u32_e32 v10, vcc, 0x50000, v18
	s_nop 1
	v_addc_co_u32_e32 v11, vcc, 0, v19, vcc
	s_waitcnt lgkmcnt(1)
	global_store_dwordx4 v[10:11], v[2:5], off
	s_nop 1
	v_add_co_u32_e32 v2, vcc, 0x58000, v18
	s_nop 1
	v_addc_co_u32_e32 v3, vcc, 0, v19, vcc
	s_waitcnt lgkmcnt(0)
	global_store_dwordx4 v[2:3], v[6:9], off
	s_waitcnt lgkmcnt(0)
	s_barrier
	s_cbranch_scc1 .LBB0_1143
	s_andn2_b64 vcc, exec, s[0:1]
	s_cbranch_vccnz .LBB0_1142
	s_barrier
	s_branch .LBB0_1142
